# baseline (speedup 1.0000x reference)
_Z6k_gemmIN2pg6EpiResELi768EEvNS0_4GemmET_:
	s_mov_b64 s[92:93], s[0:1]
	v_mov_b32_e32 v250, v0
	s_mov_b32 s94, 0
.Lrep8_start:
	s_load_dwordx2 s[4:5], s[0:1], 0x10
	v_readfirstlane_b32 s44, v0
	s_waitcnt lgkmcnt(0)
	s_ashr_i32 s3, s4, 31
	s_ashr_i32 s6, s5, 31
	s_lshr_b32 s3, s3, 24
	s_lshr_b32 s6, s6, 24
	s_add_i32 s3, s4, s3
	s_add_i32 s4, s5, s6
	s_ashr_i32 s3, s3, 8
	s_ashr_i32 s33, s4, 8
	s_mul_i32 s6, s33, s3
	s_cmp_ge_i32 s2, s6
	s_cbranch_scc1 .LBB8_32
	s_ashr_i32 s7, s6, 31
	s_lshr_b32 s4, s7, 29
	s_add_i32 s4, s6, s4
	s_ashr_i32 s45, s4, 3
	s_and_b32 s4, s4, -8
	s_ashr_i32 s47, s2, 31
	s_sub_i32 s46, s6, s4
	s_lshr_b32 s4, s47, 29
	s_add_i32 s10, s2, s4
	s_and_b32 s4, s10, -8
	s_sub_i32 s4, s2, s4
	s_add_i32 s48, s45, 1
	s_cmp_ge_i32 s4, s46
	s_mul_i32 s49, s48, s46
	s_cbranch_scc0 .LBB8_3
	s_sub_i32 s8, s4, s46
	s_mul_i32 s8, s8, s45
	s_add_i32 s20, s8, s49
	s_ashr_i32 s21, s10, 3
	s_cbranch_execz .LBB8_4
	s_branch .LBB8_5

.LBB8_31:
	s_barrier
	s_add_i32 s94, s94, 1
	s_cmp_lt_u32 s94, 2
	s_cbranch_scc0 .LBB8_32
	s_mov_b64 s[0:1], s[92:93]
	v_mov_b32_e32 v0, v250
	s_branch .Lrep8_start
.LBB8_32:
	s_endpgm
	s_endpgm
	s_endpgm
	s_endpgm
	s_endpgm
	s_endpgm
	s_endpgm
	s_endpgm
	s_endpgm
	s_endpgm
	s_endpgm
	s_endpgm
	s_endpgm
	s_endpgm
	s_endpgm
	s_endpgm

	.amdhsa_kernel _Z6k_gemmIN2pg6EpiResELi768EEvNS0_4GemmET_
		.amdhsa_group_segment_fixed_size 0
		.amdhsa_private_segment_fixed_size 0
		.amdhsa_kernarg_size 344
		.amdhsa_user_sgpr_count 2
		.amdhsa_user_sgpr_dispatch_ptr 0
		.amdhsa_user_sgpr_queue_ptr 0
		.amdhsa_user_sgpr_kernarg_segment_ptr 1
		.amdhsa_user_sgpr_dispatch_id 0
		.amdhsa_user_sgpr_kernarg_preload_length 0
		.amdhsa_user_sgpr_kernarg_preload_offset 0
		.amdhsa_user_sgpr_private_segment_size 0
		.amdhsa_uses_dynamic_stack 0
		.amdhsa_enable_private_segment 0
		.amdhsa_system_sgpr_workgroup_id_x 1
		.amdhsa_system_sgpr_workgroup_id_y 0
		.amdhsa_system_sgpr_workgroup_id_z 0
		.amdhsa_system_sgpr_workgroup_info 0
		.amdhsa_system_vgpr_workitem_id 0
		.amdhsa_next_free_vgpr 254
		.amdhsa_next_free_sgpr 95
		.amdhsa_accum_offset 256
		.amdhsa_reserve_vcc 1
		.amdhsa_float_round_mode_32 0
		.amdhsa_float_round_mode_16_64 0
		.amdhsa_float_denorm_mode_32 3
		.amdhsa_float_denorm_mode_16_64 3
		.amdhsa_dx10_clamp 1
		.amdhsa_ieee_mode 1
		.amdhsa_fp16_overflow 0
		.amdhsa_tg_split 0
		.amdhsa_exception_fp_ieee_invalid_op 0
		.amdhsa_exception_fp_denorm_src 0
		.amdhsa_exception_fp_ieee_div_zero 0
		.amdhsa_exception_fp_ieee_overflow 0
		.amdhsa_exception_fp_ieee_underflow 0
		.amdhsa_exception_fp_ieee_inexact 0
		.amdhsa_exception_int_div_zero 0
	.end_amdhsa_kernel

amdhsa.kernels:
  - .agpr_count:     16
    .args:
      - .actual_access:  read_only
        .address_space:  global
        .offset:         0
        .size:           8
        .value_kind:     global_buffer
      - .actual_access:  read_only
        .address_space:  global
        .offset:         8
        .size:           8
        .value_kind:     global_buffer
      - .actual_access:  write_only
        .address_space:  global
        .offset:         16
        .size:           8
        .value_kind:     global_buffer
    .group_segment_fixed_size: 45056
    .kernarg_segment_align: 8
    .kernarg_segment_size: 24
    .language:       OpenCL C
    .language_version:
      - 2
      - 0
    .max_flat_workgroup_size: 256
    .name:           _Z6k_attnPKDF16_PKfPDF16_
    .private_segment_fixed_size: 0
    .sgpr_count:     16
    .sgpr_spill_count: 0
    .symbol:         _Z6k_attnPKDF16_PKfPDF16_.kd
    .uniform_work_group_size: 1
    .uses_dynamic_stack: false
    .vgpr_count:     84
    .vgpr_spill_count: 0
    .wavefront_size: 64
  - .agpr_count:     0
    .args:
      - .actual_access:  read_only
        .address_space:  global
        .offset:         0
        .size:           8
        .value_kind:     global_buffer
      - .actual_access:  read_only
        .address_space:  global
        .offset:         8
        .size:           8
        .value_kind:     global_buffer
      - .actual_access:  write_only
        .address_space:  global
        .offset:         16
        .size:           8
        .value_kind:     global_buffer
      - .actual_access:  write_only
        .address_space:  global
        .offset:         24
        .size:           8
        .value_kind:     global_buffer
      - .actual_access:  write_only
        .address_space:  global
        .offset:         32
        .size:           8
        .value_kind:     global_buffer
      - .actual_access:  write_only
        .address_space:  global
        .offset:         40
        .size:           8
        .value_kind:     global_buffer
    .group_segment_fixed_size: 0
    .kernarg_segment_align: 8
    .kernarg_segment_size: 48
    .language:       OpenCL C
    .language_version:
      - 2
      - 0
    .max_flat_workgroup_size: 256
    .name:           _Z11k_prep_miscPKiPKfPfPDv2_fS3_S3_
    .private_segment_fixed_size: 0
    .sgpr_count:     16
    .sgpr_spill_count: 0
    .symbol:         _Z11k_prep_miscPKiPKfPfPDv2_fS3_S3_.kd
    .uniform_work_group_size: 1
    .uses_dynamic_stack: false
    .vgpr_count:     6
    .vgpr_spill_count: 0
    .wavefront_size: 64
  - .agpr_count:     0
    .args:
      - .actual_access:  read_only
        .address_space:  global
        .offset:         0
        .size:           8
        .value_kind:     global_buffer
      - .actual_access:  write_only
        .address_space:  global
        .offset:         8
        .size:           8
        .value_kind:     global_buffer
    .group_segment_fixed_size: 0
    .kernarg_segment_align: 8
    .kernarg_segment_size: 16
    .language:       OpenCL C
    .language_version:
      - 2
      - 0
    .max_flat_workgroup_size: 256
    .name:           _Z7k_cvt_xPKfPDF16_
    .private_segment_fixed_size: 0
    .sgpr_count:     14
    .sgpr_spill_count: 0
    .symbol:         _Z7k_cvt_xPKfPDF16_.kd
    .uniform_work_group_size: 1
    .uses_dynamic_stack: false
    .vgpr_count:     12
    .vgpr_spill_count: 0
    .wavefront_size: 64
  - .agpr_count:     0
    .args:
      - .offset:         0
        .size:           176
        .value_kind:     by_value
    .group_segment_fixed_size: 9216
    .kernarg_segment_align: 8
    .kernarg_segment_size: 176
    .language:       OpenCL C
    .language_version:
      - 2
      - 0
    .max_flat_workgroup_size: 256
    .name:           _Z8k_wtrans8PrepArgs
    .private_segment_fixed_size: 0
    .sgpr_count:     44
    .sgpr_spill_count: 0
    .symbol:         _Z8k_wtrans8PrepArgs.kd
    .uniform_work_group_size: 1
    .uses_dynamic_stack: false
    .vgpr_count:     18
    .vgpr_spill_count: 0
    .wavefront_size: 64
  - .agpr_count:     0
    .args:
      - .offset:         0
        .size:           176
        .value_kind:     by_value
      - .actual_access:  read_only
        .address_space:  global
        .offset:         176
        .size:           8
        .value_kind:     global_buffer
      - .actual_access:  read_only
        .address_space:  global
        .offset:         184
        .size:           8
        .value_kind:     global_buffer
    .group_segment_fixed_size: 2048
    .kernarg_segment_align: 8
    .kernarg_segment_size: 192
    .language:       OpenCL C
    .language_version:
      - 2
      - 0
    .max_flat_workgroup_size: 256
    .name:           _Z8k_colvec8PrepArgsPKfS1_
    .private_segment_fixed_size: 0
    .sgpr_count:     38
    .sgpr_spill_count: 0
    .symbol:         _Z8k_colvec8PrepArgsPKfS1_.kd
    .uniform_work_group_size: 1
    .uses_dynamic_stack: false
    .vgpr_count:     114
    .vgpr_spill_count: 0
    .wavefront_size: 64
  - .agpr_count:     0
    .args:
      - .actual_access:  read_only
        .address_space:  global
        .offset:         0
        .size:           8
        .value_kind:     global_buffer
      - .actual_access:  write_only
        .address_space:  global
        .offset:         8
        .size:           8
        .value_kind:     global_buffer
    .group_segment_fixed_size: 0
    .kernarg_segment_align: 8
    .kernarg_segment_size: 16
    .language:       OpenCL C
    .language_version:
      - 2
      - 0
    .max_flat_workgroup_size: 256
    .name:           _Z9k_rowstatPKDv2_fPS_
    .private_segment_fixed_size: 0
    .sgpr_count:     14
    .sgpr_spill_count: 0
    .symbol:         _Z9k_rowstatPKDv2_fPS_.kd
    .uniform_work_group_size: 1
    .uses_dynamic_stack: false
    .vgpr_count:     28
    .vgpr_spill_count: 0
    .wavefront_size: 64
  - .agpr_count:     0
    .args:
      - .actual_access:  read_only
        .address_space:  global
        .offset:         0
        .size:           8
        .value_kind:     global_buffer
      - .actual_access:  read_only
        .address_space:  global
        .offset:         8
        .size:           8
        .value_kind:     global_buffer
      - .actual_access:  read_only
        .address_space:  global
        .offset:         16
        .size:           8
        .value_kind:     global_buffer
      - .actual_access:  read_only
        .address_space:  global
        .offset:         24
        .size:           8
        .value_kind:     global_buffer
      - .actual_access:  write_only
        .address_space:  global
        .offset:         32
        .size:           8
        .value_kind:     global_buffer
    .group_segment_fixed_size: 0
    .kernarg_segment_align: 8
    .kernarg_segment_size: 40
    .language:       OpenCL C
    .language_version:
      - 2
      - 0
    .max_flat_workgroup_size: 256
    .name:           _Z10k_final_lnPKDF16_PKDv2_fPKfS5_Pf
    .private_segment_fixed_size: 0
    .sgpr_count:     19
    .sgpr_spill_count: 0
    .symbol:         _Z10k_final_lnPKDF16_PKDv2_fPKfS5_Pf.kd
    .uniform_work_group_size: 1
    .uses_dynamic_stack: false
    .vgpr_count:     19
    .vgpr_spill_count: 0
    .wavefront_size: 64
  - .agpr_count:     0
    .args:
      - .offset:         0
        .size:           32
        .value_kind:     by_value
      - .offset:         32
        .size:           32
        .value_kind:     by_value
      - .offset:         64
        .size:           4
        .value_kind:     hidden_block_count_x
      - .offset:         68
        .size:           4
        .value_kind:     hidden_block_count_y
      - .offset:         72
        .size:           4
        .value_kind:     hidden_block_count_z
      - .offset:         76
        .size:           2
        .value_kind:     hidden_group_size_x
      - .offset:         78
        .size:           2
        .value_kind:     hidden_group_size_y
      - .offset:         80
        .size:           2
        .value_kind:     hidden_group_size_z
      - .offset:         82
        .size:           2
        .value_kind:     hidden_remainder_x
      - .offset:         84
        .size:           2
        .value_kind:     hidden_remainder_y
      - .offset:         86
        .size:           2
        .value_kind:     hidden_remainder_z
      - .offset:         104
        .size:           8
        .value_kind:     hidden_global_offset_x
      - .offset:         112
        .size:           8
        .value_kind:     hidden_global_offset_y
      - .offset:         120
        .size:           8
        .value_kind:     hidden_global_offset_z
      - .offset:         128
        .size:           2
        .value_kind:     hidden_grid_dims
      - .offset:         184
        .size:           4
        .value_kind:     hidden_dynamic_lds_size
    .group_segment_fixed_size: 0
    .kernarg_segment_align: 8
    .kernarg_segment_size: 320
    .language:       OpenCL C
    .language_version:
      - 2
      - 0
    .max_flat_workgroup_size: 512
    .name:           _Z6k_gemmIN2pg6EpiLinILi0EEELi768EEvNS0_4GemmET_
    .private_segment_fixed_size: 0
    .sgpr_count:     83
    .sgpr_spill_count: 0
    .symbol:         _Z6k_gemmIN2pg6EpiLinILi0EEELi768EEvNS0_4GemmET_.kd
    .uniform_work_group_size: 1
    .uses_dynamic_stack: false
    .vgpr_count:     254
    .vgpr_spill_count: 0
    .wavefront_size: 64
  - .agpr_count:     0
    .args:
      - .offset:         0
        .size:           32
        .value_kind:     by_value
      - .offset:         32
        .size:           56
        .value_kind:     by_value
      - .offset:         88
        .size:           4
        .value_kind:     hidden_block_count_x
      - .offset:         92
        .size:           4
        .value_kind:     hidden_block_count_y
      - .offset:         96
        .size:           4
        .value_kind:     hidden_block_count_z
      - .offset:         100
        .size:           2
        .value_kind:     hidden_group_size_x
      - .offset:         102
        .size:           2
        .value_kind:     hidden_group_size_y
      - .offset:         104
        .size:           2
        .value_kind:     hidden_group_size_z
      - .offset:         106
        .size:           2
        .value_kind:     hidden_remainder_x
      - .offset:         108
        .size:           2
        .value_kind:     hidden_remainder_y
      - .offset:         110
        .size:           2
        .value_kind:     hidden_remainder_z
      - .offset:         128
        .size:           8
        .value_kind:     hidden_global_offset_x
      - .offset:         136
        .size:           8
        .value_kind:     hidden_global_offset_y
      - .offset:         144
        .size:           8
        .value_kind:     hidden_global_offset_z
      - .offset:         152
        .size:           2
        .value_kind:     hidden_grid_dims
      - .offset:         208
        .size:           4
        .value_kind:     hidden_dynamic_lds_size
    .group_segment_fixed_size: 0
    .kernarg_segment_align: 8
    .kernarg_segment_size: 344
    .language:       OpenCL C
    .language_version:
      - 2
      - 0
    .max_flat_workgroup_size: 512
    .name:           _Z6k_gemmIN2pg6EpiResELi768EEvNS0_4GemmET_
    .private_segment_fixed_size: 0
    .sgpr_count:     101
    .sgpr_spill_count: 0
    .symbol:         _Z6k_gemmIN2pg6EpiResELi768EEvNS0_4GemmET_.kd
    .uniform_work_group_size: 1
    .uses_dynamic_stack: false
    .vgpr_count:     254
    .vgpr_spill_count: 0
    .wavefront_size: 64
  - .agpr_count:     0
    .args:
      - .offset:         0
        .size:           32
        .value_kind:     by_value
      - .offset:         32
        .size:           32
        .value_kind:     by_value
      - .offset:         64
        .size:           4
        .value_kind:     hidden_block_count_x
      - .offset:         68
        .size:           4
        .value_kind:     hidden_block_count_y
      - .offset:         72
        .size:           4
        .value_kind:     hidden_block_count_z
      - .offset:         76
        .size:           2
        .value_kind:     hidden_group_size_x
      - .offset:         78
        .size:           2
        .value_kind:     hidden_group_size_y
      - .offset:         80
        .size:           2
        .value_kind:     hidden_group_size_z
      - .offset:         82
        .size:           2
        .value_kind:     hidden_remainder_x
      - .offset:         84
        .size:           2
        .value_kind:     hidden_remainder_y
      - .offset:         86
        .size:           2
        .value_kind:     hidden_remainder_z
      - .offset:         104
        .size:           8
        .value_kind:     hidden_global_offset_x
      - .offset:         112
        .size:           8
        .value_kind:     hidden_global_offset_y
      - .offset:         120
        .size:           8
        .value_kind:     hidden_global_offset_z
      - .offset:         128
        .size:           2
        .value_kind:     hidden_grid_dims
      - .offset:         184
        .size:           4
        .value_kind:     hidden_dynamic_lds_size
    .group_segment_fixed_size: 0
    .kernarg_segment_align: 8
    .kernarg_segment_size: 320
    .language:       OpenCL C
    .language_version:
      - 2
      - 0
    .max_flat_workgroup_size: 512
    .name:           _Z6k_gemmIN2pg6EpiLinILi1EEELi768EEvNS0_4GemmET_
    .private_segment_fixed_size: 0
    .sgpr_count:     83
    .sgpr_spill_count: 0
    .symbol:         _Z6k_gemmIN2pg6EpiLinILi1EEELi768EEvNS0_4GemmET_.kd
    .uniform_work_group_size: 1
    .uses_dynamic_stack: false
    .vgpr_count:     254
    .vgpr_spill_count: 0
    .wavefront_size: 64
  - .agpr_count:     0
    .args:
      - .offset:         0
        .size:           32
        .value_kind:     by_value
      - .offset:         32
        .size:           56
        .value_kind:     by_value
      - .offset:         88
        .size:           4
        .value_kind:     hidden_block_count_x
      - .offset:         92
        .size:           4
        .value_kind:     hidden_block_count_y
      - .offset:         96
        .size:           4
        .value_kind:     hidden_block_count_z
      - .offset:         100
        .size:           2
        .value_kind:     hidden_group_size_x
      - .offset:         102
        .size:           2
        .value_kind:     hidden_group_size_y
      - .offset:         104
        .size:           2
        .value_kind:     hidden_group_size_z
      - .offset:         106
        .size:           2
        .value_kind:     hidden_remainder_x
      - .offset:         108
        .size:           2
        .value_kind:     hidden_remainder_y
      - .offset:         110
        .size:           2
        .value_kind:     hidden_remainder_z
      - .offset:         128
        .size:           8
        .value_kind:     hidden_global_offset_x
      - .offset:         136
        .size:           8
        .value_kind:     hidden_global_offset_y
      - .offset:         144
        .size:           8
        .value_kind:     hidden_global_offset_z
      - .offset:         152
        .size:           2
        .value_kind:     hidden_grid_dims
      - .offset:         208
        .size:           4
        .value_kind:     hidden_dynamic_lds_size
    .group_segment_fixed_size: 0
    .kernarg_segment_align: 8
    .kernarg_segment_size: 344
    .language:       OpenCL C
    .language_version:
      - 2
      - 0
    .max_flat_workgroup_size: 512
    .name:           _Z6k_gemmIN2pg6EpiResELi3072EEvNS0_4GemmET_
    .private_segment_fixed_size: 0
    .sgpr_count:     97
    .sgpr_spill_count: 0
    .symbol:         _Z6k_gemmIN2pg6EpiResELi3072EEvNS0_4GemmET_.kd
    .uniform_work_group_size: 1
    .uses_dynamic_stack: false
    .vgpr_count:     250
    .vgpr_spill_count: 0
    .wavefront_size: 64
